# speedup vs baseline: 1.0447x; 1.0014x over previous
.LBB2_1:
	v_add_u32_e32 v130, s26, v206
	ds_read_b64_tr_b16 v[178:179], v130 offset:24576
	ds_read_b64_tr_b16 v[180:181], v130 offset:25600
	s_waitcnt lgkmcnt(9)
	v_mfma_f32_32x32x16_f16 v[98:113], v[82:85], v[154:157], v[34:49]
	v_add_f32_e32 v86, v66, v67
	v_add_f32_e32 v86, v68, v86
	v_add_f32_e32 v86, v69, v86
	v_add_f32_e32 v86, v70, v86
	v_add_f32_e32 v86, v71, v86
	v_cvt_pk_f16_f32 v158, v66, v67
	v_cvt_pk_f16_f32 v159, v68, v69
	v_add_u32_e32 v182, s26, v207
	ds_read_b64_tr_b16 v[174:175], v182 offset:24576
	ds_read_b64_tr_b16 v[176:177], v182 offset:25600
	v_add_f32_e32 v66, v72, v86
	s_waitcnt lgkmcnt(10)
	v_mfma_f32_32x32x16_f16 v[82:97], v[170:173], v[154:157], v[34:49]
	v_add_f32_e32 v66, v73, v66
	v_add_f32_e32 v66, v74, v66
	v_add_f32_e32 v66, v75, v66
	v_cvt_pk_f16_f32 v160, v70, v71
	v_cvt_pk_f16_f32 v161, v72, v73
	ds_read_b64_tr_b16 v[170:171], v130 offset:26624
	ds_read_b64_tr_b16 v[172:173], v130 offset:27648
	s_waitcnt lgkmcnt(11)
	v_mfma_f32_32x32x16_f16 v[98:113], v[166:169], v[146:149], v[98:113]
	v_add_f32_e32 v66, v76, v66
	v_add_f32_e32 v66, v77, v66
	v_add_f32_e32 v66, v78, v66
	v_add_f32_e32 v66, v79, v66
	v_cvt_pk_f16_f32 v150, v74, v75
	v_cvt_pk_f16_f32 v151, v76, v77
	ds_read_b64_tr_b16 v[74:75], v182 offset:26624
	ds_read_b64_tr_b16 v[76:77], v182 offset:27648
	s_waitcnt lgkmcnt(12)
	v_mfma_f32_32x32x16_f16 v[82:97], v[162:165], v[146:149], v[82:97]
	v_add_f32_e32 v66, v80, v66
	v_add_f32_e32 v66, v81, v66
	v_add_f32_e32 v66, v50, v66
	v_add_f32_e32 v66, v51, v66
	v_cvt_pk_f16_f32 v152, v78, v79
	v_cvt_pk_f16_f32 v153, v80, v81
	ds_read_b64_tr_b16 v[70:71], v130 offset:28672
	ds_read_b64_tr_b16 v[72:73], v130 offset:29696
	s_waitcnt lgkmcnt(13)
	v_mfma_f32_32x32x16_f16 v[98:113], v[126:129], v[138:141], v[98:113]
	v_add_f32_e32 v66, v52, v66
	v_add_f32_e32 v66, v53, v66
	v_add_f32_e32 v66, v54, v66
	v_add_f32_e32 v78, v55, v66
	v_cvt_pk_f16_f32 v142, v50, v51
	v_cvt_pk_f16_f32 v143, v52, v53
	ds_read_b64_tr_b16 v[66:67], v182 offset:28672
	ds_read_b64_tr_b16 v[68:69], v182 offset:29696
	s_waitcnt lgkmcnt(14)
	v_mfma_f32_32x32x16_f16 v[82:97], v[122:125], v[138:141], v[82:97]
	v_add_f32_e32 v50, v56, v78
	v_add_f32_e32 v50, v57, v50
	v_add_f32_e32 v50, v58, v50
	v_add_f32_e32 v50, v59, v50
	v_cvt_pk_f16_f32 v144, v54, v55
	v_cvt_pk_f16_f32 v145, v56, v57
	ds_read_b64_tr_b16 v[54:55], v130 offset:30720
	ds_read_b64_tr_b16 v[56:57], v130 offset:31744
	s_waitcnt lgkmcnt(14)
	v_mfma_f32_32x32x16_f16 v[98:113], v[118:121], v[134:137], v[98:113]
	v_add_f32_e32 v50, v60, v50
	v_add_f32_e32 v50, v61, v50
	v_add_f32_e32 v50, v62, v50
	v_add_f32_e32 v78, v63, v50
	v_cvt_pk_f16_f32 v130, v58, v59
	v_cvt_pk_f16_f32 v131, v60, v61
	ds_read_b64_tr_b16 v[50:51], v182 offset:30720
	ds_read_b64_tr_b16 v[52:53], v182 offset:31744
	v_mfma_f32_32x32x16_f16 v[82:97], v[114:117], v[134:137], v[82:97]
	v_add_f32_e32 v58, v64, v78
	v_add_f32_e32 v60, v65, v58
	v_cvt_pk_f16_f32 v132, v62, v63
	v_cvt_pk_f16_f32 v133, v64, v65
	v_lshl_add_u64 v[58:59], v[188:189], 0, s[24:25]
	s_add_i32 s26, s42, s36
	s_mov_b32 m0, s26
	s_nop 0
	global_load_lds_dwordx4 v[58:59], off
	v_lshl_add_u64 v[58:59], v[196:197], 0, s[20:21]
	s_add_i32 s26, s39, s35
	s_mov_b32 m0, s26
	s_nop 0
	global_load_lds_dwordx4 v[58:59], off
	v_max_f32_e32 v58, v98, v99
	v_max3_f32 v59, v100, v101, v83
	v_max3_f32 v58, v58, v82, v84
	v_max3_f32 v58, v58, v85, v102
	v_max3_f32 v59, v59, v104, v105
	v_max3_f32 v58, v58, v103, v86
	v_max3_f32 v59, v59, v88, v89
	v_max3_f32 v58, v58, v87, v106
	v_max3_f32 v59, v59, v108, v109
	v_max3_f32 v58, v58, v107, v90
	v_max3_f32 v59, v59, v92, v93
	v_max3_f32 v58, v58, v91, v110
	v_max3_f32 v59, v59, v112, v113
	v_max3_f32 v58, v58, v111, v94
	v_max3_f32 v59, v59, v96, v97
	v_max3_f32 v58, v58, v95, v59
	v_mov_b32_e32 v59, v58
	v_add_f32_e32 v198, v183, v60
	s_nop 0
	v_permlane32_swap_b32_e32 v58, v59
	v_max_f32_e32 v58, v58, v59
	v_cmp_lt_f32_e32 vcc, s41, v58
	s_cmp_lg_u64 vcc, 0
	s_cselect_b64 s[26:27], -1, 0
	s_cbranch_vccnz .LBB2_9

.LBB2_4:
	s_add_i32 s26, s39, 0x2000
	s_cmpk_lg_i32 s39, 0x4000
	s_cselect_b32 s43, s26, 0
	v_add_u32_e32 v130, s42, v206
	ds_read_b64_tr_b16 v[126:127], v130 offset:24576
	ds_read_b64_tr_b16 v[128:129], v130 offset:25600
	s_waitcnt lgkmcnt(9)
	v_mfma_f32_32x32x16_f16 v[66:81], v[58:61], v[154:157], v[34:49]
	v_add_f32_e32 v50, v98, v99
	v_add_f32_e32 v50, v100, v50
	v_add_f32_e32 v50, v101, v50
	v_add_f32_e32 v50, v102, v50
	v_add_f32_e32 v50, v103, v50
	v_cvt_pk_f16_f32 v158, v98, v99
	v_cvt_pk_f16_f32 v159, v100, v101
	v_add_u32_e32 v199, s42, v207
	ds_read_b64_tr_b16 v[122:123], v199 offset:24576
	ds_read_b64_tr_b16 v[124:125], v199 offset:25600
	v_add_f32_e32 v50, v104, v50
	v_add_f32_e32 v50, v105, v50
	v_add_f32_e32 v50, v106, v50
	v_add_f32_e32 v98, v107, v50
	s_waitcnt lgkmcnt(10)
	v_mfma_f32_32x32x16_f16 v[50:65], v[114:117], v[154:157], v[34:49]
	v_cvt_pk_f16_f32 v160, v102, v103
	v_cvt_pk_f16_f32 v161, v104, v105
	ds_read_b64_tr_b16 v[118:119], v130 offset:26624
	ds_read_b64_tr_b16 v[120:121], v130 offset:27648
	s_waitcnt lgkmcnt(11)
	v_mfma_f32_32x32x16_f16 v[66:81], v[182:185], v[146:149], v[66:81]
	v_add_f32_e32 v98, v108, v98
	v_add_f32_e32 v98, v109, v98
	v_add_f32_e32 v98, v110, v98
	v_add_f32_e32 v98, v111, v98
	v_cvt_pk_f16_f32 v150, v106, v107
	v_cvt_pk_f16_f32 v151, v108, v109
	ds_read_b64_tr_b16 v[114:115], v199 offset:26624
	ds_read_b64_tr_b16 v[116:117], v199 offset:27648
	s_waitcnt lgkmcnt(12)
	v_mfma_f32_32x32x16_f16 v[50:65], v[174:177], v[146:149], v[50:65]
	v_add_f32_e32 v98, v112, v98
	v_add_f32_e32 v98, v113, v98
	v_add_f32_e32 v98, v82, v98
	v_add_f32_e32 v98, v83, v98
	v_cvt_pk_f16_f32 v152, v110, v111
	v_cvt_pk_f16_f32 v153, v112, v113
	ds_read_b64_tr_b16 v[106:107], v130 offset:28672
	ds_read_b64_tr_b16 v[108:109], v130 offset:29696
	s_waitcnt lgkmcnt(13)
	v_mfma_f32_32x32x16_f16 v[66:81], v[178:181], v[138:141], v[66:81]
	v_add_f32_e32 v98, v84, v98
	v_add_f32_e32 v98, v85, v98
	v_add_f32_e32 v98, v86, v98
	v_add_f32_e32 v98, v87, v98
	v_cvt_pk_f16_f32 v142, v82, v83
	v_cvt_pk_f16_f32 v143, v84, v85
	ds_read_b64_tr_b16 v[102:103], v199 offset:28672
	ds_read_b64_tr_b16 v[104:105], v199 offset:29696
	s_waitcnt lgkmcnt(14)
	v_mfma_f32_32x32x16_f16 v[50:65], v[166:169], v[138:141], v[50:65]
	v_add_f32_e32 v82, v88, v98
	v_add_f32_e32 v82, v89, v82
	v_add_f32_e32 v82, v90, v82
	v_add_f32_e32 v82, v91, v82
	v_cvt_pk_f16_f32 v144, v86, v87
	v_cvt_pk_f16_f32 v145, v88, v89
	ds_read_b64_tr_b16 v[98:99], v130 offset:30720
	ds_read_b64_tr_b16 v[100:101], v130 offset:31744
	s_waitcnt lgkmcnt(14)
	v_mfma_f32_32x32x16_f16 v[66:81], v[170:173], v[134:137], v[66:81]
	v_add_f32_e32 v82, v92, v82
	v_add_f32_e32 v82, v93, v82
	v_add_f32_e32 v82, v94, v82
	v_add_f32_e32 v82, v95, v82
	v_cvt_pk_f16_f32 v130, v90, v91
	v_cvt_pk_f16_f32 v131, v92, v93
	ds_read_b64_tr_b16 v[86:87], v199 offset:30720
	ds_read_b64_tr_b16 v[88:89], v199 offset:31744
	v_mfma_f32_32x32x16_f16 v[50:65], v[162:165], v[134:137], v[50:65]
	v_add_f32_e32 v82, v96, v82
	v_add_f32_e32 v84, v97, v82
	v_cvt_pk_f16_f32 v132, v94, v95
	v_cvt_pk_f16_f32 v133, v96, v97
	v_lshl_add_u64 v[82:83], v[188:189], 0, s[2:3]
	s_add_i32 s26, s39, s36
	s_mov_b32 m0, s26
	s_nop 0
	global_load_lds_dwordx4 v[82:83], off
	v_max_f32_e32 v82, v66, v67
	s_nop 1
	v_max3_f32 v83, v68, v69, v51
	v_max3_f32 v82, v82, v50, v52
	v_max3_f32 v82, v82, v53, v70
	v_max3_f32 v83, v83, v72, v73
	v_max3_f32 v82, v82, v71, v54
	v_max3_f32 v83, v83, v56, v57
	v_max3_f32 v82, v82, v55, v74
	v_max3_f32 v83, v83, v76, v77
	v_max3_f32 v82, v82, v75, v58
	v_max3_f32 v83, v83, v60, v61
	v_max3_f32 v82, v82, v59, v78
	v_max3_f32 v83, v83, v80, v81
	v_max3_f32 v82, v82, v79, v62
	v_max3_f32 v83, v83, v64, v65
	v_max3_f32 v82, v82, v63, v83
	v_mov_b32_e32 v83, v82
	v_add_f32_e32 v183, v198, v84
	s_nop 0
	v_permlane32_swap_b32_e32 v82, v83
	v_max_f32_e32 v82, v82, v83
	v_lshl_add_u64 v[196:197], v[196:197], 0, s[22:23]
	s_add_i32 s26, s43, s35
	s_mov_b32 m0, s26
	s_nop 0
	global_load_lds_dwordx4 v[196:197], off
	v_cmp_lt_f32_e32 vcc, s41, v82
	s_cmp_lg_u64 vcc, 0
	s_cselect_b64 s[26:27], -1, 0
	s_cbranch_vccnz .LBB2_12
